# speedup vs baseline: 1.0224x; 1.0183x over previous
.LBB2_10:
	s_or_b64 exec, exec, s[10:11]
	v_mov_b32_e32 v52, 0x7bff7bff
	v_mov_b32_e32 v99, 0x7bff7bff
	v_mov_b32_e32 v98, 0x7bff7bff
	v_mov_b32_e32 v103, 0x7bff7bff
	v_mov_b32_e32 v100, 0xfbfffbff
	v_mov_b32_e32 v101, 0xfbfffbff
	v_mov_b32_e32 v105, 0xfbfffbff
	v_mov_b32_e32 v104, 0xfbfffbff
	v_mov_b32_e32 v62, 0
	v_mov_b32_e32 v63, 0
	v_mov_b32_e32 v64, 0
	v_mov_b32_e32 v65, 0
	v_mov_b32_e32 v66, 0
	v_mov_b32_e32 v67, 0
	v_mov_b32_e32 v68, 0
	v_mov_b32_e32 v69, 0
	v_mov_b32_e32 v70, 0
	v_mov_b32_e32 v71, 0
	v_mov_b32_e32 v72, 0
	v_mov_b32_e32 v73, 0
	v_mov_b32_e32 v74, 0
	v_mov_b32_e32 v75, 0
	v_mov_b32_e32 v76, 0
	v_mov_b32_e32 v77, 0
	v_cmp_lt_i32_e64 s[10:11], v50, v97
	v_mov_b32_e32 v91, v97
	v_and_b32_e32 v92, 3, v50
	s_waitcnt lgkmcnt(0)
	v_cndmask_b32_e64 v10, v11, v10, s[10:11]
	v_add_u32_e32 v92, 8, v92
	v_add_u32_e32 v93, -1, v97
	v_cndmask_b32_e64 v81, 0, v10, s[0:1]
	v_cndmask_b32_e64 v93, 0, v93, s[0:1]
	v_cndmask_b32_e64 v94, 0, v78, s[0:1]
	v_lshlrev_b32_e32 v81, 7, v81
	v_min_i32_e32 v116, v92, v93
	v_add_u32_e32 v117, 4, v92
	v_min_i32_e32 v117, v117, v93
	v_add_lshl_u32 v116, v116, v94, 2
	v_add_lshl_u32 v117, v117, v94, 2
	global_load_dword v87, v116, s[24:25]
	global_load_dword v88, v117, s[24:25]
	v_add_u32_e32 v92, 8, v92
	v_mov_b32_e32 v89, v81
	v_mov_b32_e32 v90, v81
	s_nop 1
	v_mov_b32_dpp v89, v81 row_shr:4 row_mask:0xf bank_mask:0xa
	v_mov_b32_dpp v90, v81 row_shl:4 row_mask:0xf bank_mask:0x5
	s_mov_b64 s[78:79], 0xff
	v_cmp_gt_i32_e64 s[44:45], v91, 0
	v_cmp_gt_i32_e64 s[46:47], v91, 1
	v_cmp_gt_i32_e64 s[48:49], v91, 2
	v_cmp_gt_i32_e64 s[50:51], v91, 3
	v_cmp_gt_i32_e64 s[52:53], v91, 4
	v_cmp_gt_i32_e64 s[54:55], v91, 5
	v_cmp_gt_i32_e64 s[56:57], v91, 6
	v_cmp_gt_i32_e64 s[58:59], v91, 7
	s_nop 0
	v_or_b32_dpp v79, v89, v56 quad_perm:[0,0,0,0] row_mask:0xf bank_mask:0xf
	v_or_b32_dpp v80, v89, v56 quad_perm:[1,1,1,1] row_mask:0xf bank_mask:0xf
	s_or_b64 exec, s[44:45], s[78:79]
	global_load_dwordx4 v[10:13], v79, s[30:31]
	global_load_dwordx4 v[14:17], v80, s[30:31]
	s_mov_b64 exec, -1
	s_nop 0
	v_or_b32_dpp v79, v89, v56 quad_perm:[2,2,2,2] row_mask:0xf bank_mask:0xf
	v_or_b32_dpp v80, v89, v56 quad_perm:[3,3,3,3] row_mask:0xf bank_mask:0xf
	s_or_b64 exec, s[48:49], s[78:79]
	global_load_dwordx4 v[18:21], v79, s[30:31]
	global_load_dwordx4 v[22:25], v80, s[30:31]
	s_mov_b64 exec, -1
	s_nop 0
	v_or_b32_dpp v79, v90, v56 quad_perm:[0,0,0,0] row_mask:0xf bank_mask:0xf
	v_or_b32_dpp v80, v90, v56 quad_perm:[1,1,1,1] row_mask:0xf bank_mask:0xf
	s_or_b64 exec, s[52:53], s[78:79]
	global_load_dwordx4 v[26:29], v79, s[30:31]
	global_load_dwordx4 v[30:33], v80, s[30:31]
	s_mov_b64 exec, -1
	s_nop 0
	v_or_b32_dpp v79, v90, v56 quad_perm:[2,2,2,2] row_mask:0xf bank_mask:0xf
	v_or_b32_dpp v80, v90, v56 quad_perm:[3,3,3,3] row_mask:0xf bank_mask:0xf
	s_or_b64 exec, s[56:57], s[78:79]
	global_load_dwordx4 v[34:37], v79, s[30:31]
	global_load_dwordx4 v[38:41], v80, s[30:31]
	s_mov_b64 exec, -1
	v_cmp_gt_i32_e64 s[60:61], v91, 8
	s_cmp_lg_u64 s[60:61], 0
	s_cbranch_scc0 .Lpl_last_a0
.Lpl_steady_a0:
	s_waitcnt vmcnt(6)
	v_lshlrev_b32_e32 v89, 7, v87
	v_lshlrev_b32_e32 v90, 7, v88
	v_min_i32_e32 v116, v92, v93
	v_add_u32_e32 v117, 4, v92
	v_min_i32_e32 v117, v117, v93
	v_add_lshl_u32 v116, v116, v94, 2
	v_add_lshl_u32 v117, v117, v94, 2
	global_load_dword v87, v116, s[24:25]
	global_load_dword v88, v117, s[24:25]
	v_add_u32_e32 v92, 8, v92
	v_cmp_gt_i32_e64 s[62:63], v91, 8
	v_cmp_gt_i32_e64 s[64:65], v91, 9
	v_cmp_gt_i32_e64 s[66:67], v91, 10
	v_cmp_gt_i32_e64 s[68:69], v91, 11
	v_cmp_gt_i32_e64 s[70:71], v91, 12
	v_cmp_gt_i32_e64 s[72:73], v91, 13
	v_cmp_gt_i32_e64 s[74:75], v91, 14
	v_cmp_gt_i32_e64 s[76:77], v91, 15
	s_mov_b64 exec, s[44:45]
	v_pk_minimum3_f16 v52, v52, v10, v14
	v_pk_maximum3_f16 v100, v100, v10, v14
	v_pk_minimum3_f16 v99, v99, v11, v15
	v_pk_maximum3_f16 v101, v101, v11, v15
	v_pk_minimum3_f16 v98, v98, v12, v16
	v_pk_maximum3_f16 v105, v105, v12, v16
	v_pk_minimum3_f16 v103, v103, v13, v17
	v_pk_maximum3_f16 v104, v104, v13, v17
	v_pk_mul_f16 v110, v10, v10
	v_mov_b32_e32 v106, v10
	v_pk_mul_f16 v111, v11, v11
	v_mov_b32_e32 v107, v11
	v_pk_mul_f16 v112, v12, v12
	v_mov_b32_e32 v108, v12
	v_pk_mul_f16 v113, v13, v13
	v_mov_b32_e32 v109, v13
	s_mov_b64 exec, s[46:47]
	v_pk_add_f16 v106, v106, v14
	v_pk_fma_f16 v110, v14, v14, v110
	v_pk_add_f16 v107, v107, v15
	v_pk_fma_f16 v111, v15, v15, v111
	v_pk_add_f16 v108, v108, v16
	v_pk_fma_f16 v112, v16, v16, v112
	v_pk_add_f16 v109, v109, v17
	v_pk_fma_f16 v113, v17, v17, v113
	s_mov_b64 exec, -1
	s_nop 0
	v_or_b32_dpp v79, v89, v56 quad_perm:[0,0,0,0] row_mask:0xf bank_mask:0xf
	v_or_b32_dpp v80, v89, v56 quad_perm:[1,1,1,1] row_mask:0xf bank_mask:0xf
	s_or_b64 exec, s[62:63], s[78:79]
	global_load_dwordx4 v[10:13], v79, s[30:31]
	global_load_dwordx4 v[14:17], v80, s[30:31]
	s_mov_b64 exec, -1
	s_waitcnt vmcnt(8)
	s_mov_b64 exec, s[48:49]
	v_pk_minimum3_f16 v52, v52, v18, v22
	v_pk_maximum3_f16 v100, v100, v18, v22
	v_pk_minimum3_f16 v99, v99, v19, v23
	v_pk_maximum3_f16 v101, v101, v19, v23
	v_pk_minimum3_f16 v98, v98, v20, v24
	v_pk_maximum3_f16 v105, v105, v20, v24
	v_pk_minimum3_f16 v103, v103, v21, v25
	v_pk_maximum3_f16 v104, v104, v21, v25
	v_pk_add_f16 v106, v106, v18
	v_pk_fma_f16 v110, v18, v18, v110
	v_pk_add_f16 v107, v107, v19
	v_pk_fma_f16 v111, v19, v19, v111
	v_pk_add_f16 v108, v108, v20
	v_pk_fma_f16 v112, v20, v20, v112
	v_pk_add_f16 v109, v109, v21
	v_pk_fma_f16 v113, v21, v21, v113
	s_mov_b64 exec, s[50:51]
	v_pk_add_f16 v106, v106, v22
	v_pk_fma_f16 v110, v22, v22, v110
	v_pk_add_f16 v107, v107, v23
	v_pk_fma_f16 v111, v23, v23, v111
	v_pk_add_f16 v108, v108, v24
	v_pk_fma_f16 v112, v24, v24, v112
	v_pk_add_f16 v109, v109, v25
	v_pk_fma_f16 v113, v25, v25, v113
	s_mov_b64 exec, -1
	s_nop 0
	v_or_b32_dpp v79, v89, v56 quad_perm:[2,2,2,2] row_mask:0xf bank_mask:0xf
	v_or_b32_dpp v80, v89, v56 quad_perm:[3,3,3,3] row_mask:0xf bank_mask:0xf
	s_or_b64 exec, s[66:67], s[78:79]
	global_load_dwordx4 v[18:21], v79, s[30:31]
	global_load_dwordx4 v[22:25], v80, s[30:31]
	s_mov_b64 exec, -1
	s_waitcnt vmcnt(8)
	s_mov_b64 exec, s[52:53]
	v_pk_minimum3_f16 v52, v52, v26, v30
	v_pk_maximum3_f16 v100, v100, v26, v30
	v_pk_minimum3_f16 v99, v99, v27, v31
	v_pk_maximum3_f16 v101, v101, v27, v31
	v_pk_minimum3_f16 v98, v98, v28, v32
	v_pk_maximum3_f16 v105, v105, v28, v32
	v_pk_minimum3_f16 v103, v103, v29, v33
	v_pk_maximum3_f16 v104, v104, v29, v33
	v_pk_add_f16 v106, v106, v26
	v_pk_fma_f16 v110, v26, v26, v110
	v_pk_add_f16 v107, v107, v27
	v_pk_fma_f16 v111, v27, v27, v111
	v_pk_add_f16 v108, v108, v28
	v_pk_fma_f16 v112, v28, v28, v112
	v_pk_add_f16 v109, v109, v29
	v_pk_fma_f16 v113, v29, v29, v113
	s_mov_b64 exec, s[54:55]
	v_pk_add_f16 v106, v106, v30
	v_pk_fma_f16 v110, v30, v30, v110
	v_pk_add_f16 v107, v107, v31
	v_pk_fma_f16 v111, v31, v31, v111
	v_pk_add_f16 v108, v108, v32
	v_pk_fma_f16 v112, v32, v32, v112
	v_pk_add_f16 v109, v109, v33
	v_pk_fma_f16 v113, v33, v33, v113
	s_mov_b64 exec, -1
	s_nop 0
	v_or_b32_dpp v79, v90, v56 quad_perm:[0,0,0,0] row_mask:0xf bank_mask:0xf
	v_or_b32_dpp v80, v90, v56 quad_perm:[1,1,1,1] row_mask:0xf bank_mask:0xf
	s_or_b64 exec, s[70:71], s[78:79]
	global_load_dwordx4 v[26:29], v79, s[30:31]
	global_load_dwordx4 v[30:33], v80, s[30:31]
	s_mov_b64 exec, -1
	s_waitcnt vmcnt(8)
	s_mov_b64 exec, s[56:57]
	v_pk_minimum3_f16 v52, v52, v34, v38
	v_pk_maximum3_f16 v100, v100, v34, v38
	v_pk_minimum3_f16 v99, v99, v35, v39
	v_pk_maximum3_f16 v101, v101, v35, v39
	v_pk_minimum3_f16 v98, v98, v36, v40
	v_pk_maximum3_f16 v105, v105, v36, v40
	v_pk_minimum3_f16 v103, v103, v37, v41
	v_pk_maximum3_f16 v104, v104, v37, v41
	v_pk_add_f16 v106, v106, v34
	v_pk_fma_f16 v110, v34, v34, v110
	v_pk_add_f16 v107, v107, v35
	v_pk_fma_f16 v111, v35, v35, v111
	v_pk_add_f16 v108, v108, v36
	v_pk_fma_f16 v112, v36, v36, v112
	v_pk_add_f16 v109, v109, v37
	v_pk_fma_f16 v113, v37, v37, v113
	s_mov_b64 exec, s[58:59]
	v_pk_add_f16 v106, v106, v38
	v_pk_fma_f16 v110, v38, v38, v110
	v_pk_add_f16 v107, v107, v39
	v_pk_fma_f16 v111, v39, v39, v111
	v_pk_add_f16 v108, v108, v40
	v_pk_fma_f16 v112, v40, v40, v112
	v_pk_add_f16 v109, v109, v41
	v_pk_fma_f16 v113, v41, v41, v113
	s_mov_b64 exec, -1
	s_nop 0
	v_or_b32_dpp v79, v90, v56 quad_perm:[2,2,2,2] row_mask:0xf bank_mask:0xf
	v_or_b32_dpp v80, v90, v56 quad_perm:[3,3,3,3] row_mask:0xf bank_mask:0xf
	s_or_b64 exec, s[74:75], s[78:79]
	global_load_dwordx4 v[34:37], v79, s[30:31]
	global_load_dwordx4 v[38:41], v80, s[30:31]
	s_mov_b64 exec, -1
	s_mov_b64 exec, s[44:45]
	v_cvt_f32_f16_e32 v114, v106
	v_cvt_f32_f16_sdwa v115, v106 dst_sel:DWORD dst_unused:UNUSED_PAD src0_sel:WORD_1
	v_cvt_f32_f16_e32 v118, v110
	v_cvt_f32_f16_sdwa v119, v110 dst_sel:DWORD dst_unused:UNUSED_PAD src0_sel:WORD_1
	v_pk_add_f32 v[72:73], v[72:73], v[114:115]
	v_cvt_f32_f16_e32 v114, v107
	v_cvt_f32_f16_sdwa v115, v107 dst_sel:DWORD dst_unused:UNUSED_PAD src0_sel:WORD_1
	v_pk_add_f32 v[76:77], v[76:77], v[118:119]
	v_cvt_f32_f16_e32 v118, v111
	v_cvt_f32_f16_sdwa v119, v111 dst_sel:DWORD dst_unused:UNUSED_PAD src0_sel:WORD_1
	v_pk_add_f32 v[70:71], v[70:71], v[114:115]
	v_cvt_f32_f16_e32 v114, v108
	v_cvt_f32_f16_sdwa v115, v108 dst_sel:DWORD dst_unused:UNUSED_PAD src0_sel:WORD_1
	v_pk_add_f32 v[74:75], v[74:75], v[118:119]
	v_cvt_f32_f16_e32 v118, v112
	v_cvt_f32_f16_sdwa v119, v112 dst_sel:DWORD dst_unused:UNUSED_PAD src0_sel:WORD_1
	v_pk_add_f32 v[64:65], v[64:65], v[114:115]
	v_cvt_f32_f16_e32 v114, v109
	v_cvt_f32_f16_sdwa v115, v109 dst_sel:DWORD dst_unused:UNUSED_PAD src0_sel:WORD_1
	v_pk_add_f32 v[68:69], v[68:69], v[118:119]
	v_cvt_f32_f16_e32 v118, v113
	v_cvt_f32_f16_sdwa v119, v113 dst_sel:DWORD dst_unused:UNUSED_PAD src0_sel:WORD_1
	v_pk_add_f32 v[62:63], v[62:63], v[114:115]
	s_nop 0
	v_pk_add_f32 v[66:67], v[66:67], v[118:119]
	s_mov_b64 exec, -1
	s_mov_b64 s[44:45], s[62:63]
	s_mov_b64 s[46:47], s[64:65]
	s_mov_b64 s[48:49], s[66:67]
	s_mov_b64 s[50:51], s[68:69]
	s_mov_b64 s[52:53], s[70:71]
	s_mov_b64 s[54:55], s[72:73]
	s_mov_b64 s[56:57], s[74:75]
	s_mov_b64 s[58:59], s[76:77]
	v_add_u32_e32 v91, -8, v91
	v_cmp_gt_i32_e64 s[60:61], v91, 8
	s_cmp_lg_u64 s[60:61], 0
	s_cbranch_scc1 .Lpl_steady_a0
.Lpl_last_a0:
	s_waitcnt vmcnt(6)
	s_mov_b64 exec, s[44:45]
	v_pk_minimum3_f16 v52, v52, v10, v14
	v_pk_maximum3_f16 v100, v100, v10, v14
	v_pk_minimum3_f16 v99, v99, v11, v15
	v_pk_maximum3_f16 v101, v101, v11, v15
	v_pk_minimum3_f16 v98, v98, v12, v16
	v_pk_maximum3_f16 v105, v105, v12, v16
	v_pk_minimum3_f16 v103, v103, v13, v17
	v_pk_maximum3_f16 v104, v104, v13, v17
	v_pk_mul_f16 v110, v10, v10
	v_mov_b32_e32 v106, v10
	v_pk_mul_f16 v111, v11, v11
	v_mov_b32_e32 v107, v11
	v_pk_mul_f16 v112, v12, v12
	v_mov_b32_e32 v108, v12
	v_pk_mul_f16 v113, v13, v13
	v_mov_b32_e32 v109, v13
	s_mov_b64 exec, s[46:47]
	v_pk_add_f16 v106, v106, v14
	v_pk_fma_f16 v110, v14, v14, v110
	v_pk_add_f16 v107, v107, v15
	v_pk_fma_f16 v111, v15, v15, v111
	v_pk_add_f16 v108, v108, v16
	v_pk_fma_f16 v112, v16, v16, v112
	v_pk_add_f16 v109, v109, v17
	v_pk_fma_f16 v113, v17, v17, v113
	s_mov_b64 exec, -1
	s_waitcnt vmcnt(4)
	s_mov_b64 exec, s[48:49]
	v_pk_minimum3_f16 v52, v52, v18, v22
	v_pk_maximum3_f16 v100, v100, v18, v22
	v_pk_minimum3_f16 v99, v99, v19, v23
	v_pk_maximum3_f16 v101, v101, v19, v23
	v_pk_minimum3_f16 v98, v98, v20, v24
	v_pk_maximum3_f16 v105, v105, v20, v24
	v_pk_minimum3_f16 v103, v103, v21, v25
	v_pk_maximum3_f16 v104, v104, v21, v25
	v_pk_add_f16 v106, v106, v18
	v_pk_fma_f16 v110, v18, v18, v110
	v_pk_add_f16 v107, v107, v19
	v_pk_fma_f16 v111, v19, v19, v111
	v_pk_add_f16 v108, v108, v20
	v_pk_fma_f16 v112, v20, v20, v112
	v_pk_add_f16 v109, v109, v21
	v_pk_fma_f16 v113, v21, v21, v113
	s_mov_b64 exec, s[50:51]
	v_pk_add_f16 v106, v106, v22
	v_pk_fma_f16 v110, v22, v22, v110
	v_pk_add_f16 v107, v107, v23
	v_pk_fma_f16 v111, v23, v23, v111
	v_pk_add_f16 v108, v108, v24
	v_pk_fma_f16 v112, v24, v24, v112
	v_pk_add_f16 v109, v109, v25
	v_pk_fma_f16 v113, v25, v25, v113
	s_mov_b64 exec, -1
	s_waitcnt vmcnt(2)
	s_mov_b64 exec, s[52:53]
	v_pk_minimum3_f16 v52, v52, v26, v30
	v_pk_maximum3_f16 v100, v100, v26, v30
	v_pk_minimum3_f16 v99, v99, v27, v31
	v_pk_maximum3_f16 v101, v101, v27, v31
	v_pk_minimum3_f16 v98, v98, v28, v32
	v_pk_maximum3_f16 v105, v105, v28, v32
	v_pk_minimum3_f16 v103, v103, v29, v33
	v_pk_maximum3_f16 v104, v104, v29, v33
	v_pk_add_f16 v106, v106, v26
	v_pk_fma_f16 v110, v26, v26, v110
	v_pk_add_f16 v107, v107, v27
	v_pk_fma_f16 v111, v27, v27, v111
	v_pk_add_f16 v108, v108, v28
	v_pk_fma_f16 v112, v28, v28, v112
	v_pk_add_f16 v109, v109, v29
	v_pk_fma_f16 v113, v29, v29, v113
	s_mov_b64 exec, s[54:55]
	v_pk_add_f16 v106, v106, v30
	v_pk_fma_f16 v110, v30, v30, v110
	v_pk_add_f16 v107, v107, v31
	v_pk_fma_f16 v111, v31, v31, v111
	v_pk_add_f16 v108, v108, v32
	v_pk_fma_f16 v112, v32, v32, v112
	v_pk_add_f16 v109, v109, v33
	v_pk_fma_f16 v113, v33, v33, v113
	s_mov_b64 exec, -1
	s_waitcnt vmcnt(0)
	s_mov_b64 exec, s[56:57]
	v_pk_minimum3_f16 v52, v52, v34, v38
	v_pk_maximum3_f16 v100, v100, v34, v38
	v_pk_minimum3_f16 v99, v99, v35, v39
	v_pk_maximum3_f16 v101, v101, v35, v39
	v_pk_minimum3_f16 v98, v98, v36, v40
	v_pk_maximum3_f16 v105, v105, v36, v40
	v_pk_minimum3_f16 v103, v103, v37, v41
	v_pk_maximum3_f16 v104, v104, v37, v41
	v_pk_add_f16 v106, v106, v34
	v_pk_fma_f16 v110, v34, v34, v110
	v_pk_add_f16 v107, v107, v35
	v_pk_fma_f16 v111, v35, v35, v111
	v_pk_add_f16 v108, v108, v36
	v_pk_fma_f16 v112, v36, v36, v112
	v_pk_add_f16 v109, v109, v37
	v_pk_fma_f16 v113, v37, v37, v113
	s_mov_b64 exec, s[58:59]
	v_pk_add_f16 v106, v106, v38
	v_pk_fma_f16 v110, v38, v38, v110
	v_pk_add_f16 v107, v107, v39
	v_pk_fma_f16 v111, v39, v39, v111
	v_pk_add_f16 v108, v108, v40
	v_pk_fma_f16 v112, v40, v40, v112
	v_pk_add_f16 v109, v109, v41
	v_pk_fma_f16 v113, v41, v41, v113
	s_mov_b64 exec, -1
	s_mov_b64 exec, s[44:45]
	v_cvt_f32_f16_e32 v114, v106
	v_cvt_f32_f16_sdwa v115, v106 dst_sel:DWORD dst_unused:UNUSED_PAD src0_sel:WORD_1
	v_cvt_f32_f16_e32 v118, v110
	v_cvt_f32_f16_sdwa v119, v110 dst_sel:DWORD dst_unused:UNUSED_PAD src0_sel:WORD_1
	v_pk_add_f32 v[72:73], v[72:73], v[114:115]
	v_cvt_f32_f16_e32 v114, v107
	v_cvt_f32_f16_sdwa v115, v107 dst_sel:DWORD dst_unused:UNUSED_PAD src0_sel:WORD_1
	v_pk_add_f32 v[76:77], v[76:77], v[118:119]
	v_cvt_f32_f16_e32 v118, v111
	v_cvt_f32_f16_sdwa v119, v111 dst_sel:DWORD dst_unused:UNUSED_PAD src0_sel:WORD_1
	v_pk_add_f32 v[70:71], v[70:71], v[114:115]
	v_cvt_f32_f16_e32 v114, v108
	v_cvt_f32_f16_sdwa v115, v108 dst_sel:DWORD dst_unused:UNUSED_PAD src0_sel:WORD_1
	v_pk_add_f32 v[74:75], v[74:75], v[118:119]
	v_cvt_f32_f16_e32 v118, v112
	v_cvt_f32_f16_sdwa v119, v112 dst_sel:DWORD dst_unused:UNUSED_PAD src0_sel:WORD_1
	v_pk_add_f32 v[64:65], v[64:65], v[114:115]
	v_cvt_f32_f16_e32 v114, v109
	v_cvt_f32_f16_sdwa v115, v109 dst_sel:DWORD dst_unused:UNUSED_PAD src0_sel:WORD_1
	v_pk_add_f32 v[68:69], v[68:69], v[118:119]
	v_cvt_f32_f16_e32 v118, v113
	v_cvt_f32_f16_sdwa v119, v113 dst_sel:DWORD dst_unused:UNUSED_PAD src0_sel:WORD_1
	v_pk_add_f32 v[62:63], v[62:63], v[114:115]
	s_nop 0
	v_pk_add_f32 v[66:67], v[66:67], v[118:119]
	s_mov_b64 exec, -1
	s_xor_b64 s[0:1], s[4:5], -1
	s_and_saveexec_b64 s[4:5], s[6:7]
	s_xor_b64 s[4:5], exec, s[4:5]
	s_cbranch_execz .LBB2_22
	s_waitcnt vmcnt(0)
	v_cndmask_b32_e64 v6, 0, v95, s[2:3]
	v_pack_b32_f16 v13, v6, v6
	v_mov_b32_e32 v12, v13
	s_waitcnt lgkmcnt(0)
	v_mov_b32_e32 v11, v13
	v_mov_b32_e32 v10, v13

.LBB3_10:
	s_or_b64 exec, exec, s[10:11]
	v_mov_b32_e32 v52, 0x7bff7bff
	v_mov_b32_e32 v99, 0x7bff7bff
	v_mov_b32_e32 v98, 0x7bff7bff
	v_mov_b32_e32 v103, 0x7bff7bff
	v_mov_b32_e32 v100, 0xfbfffbff
	v_mov_b32_e32 v101, 0xfbfffbff
	v_mov_b32_e32 v105, 0xfbfffbff
	v_mov_b32_e32 v104, 0xfbfffbff
	v_mov_b32_e32 v62, 0
	v_mov_b32_e32 v63, 0
	v_mov_b32_e32 v64, 0
	v_mov_b32_e32 v65, 0
	v_mov_b32_e32 v66, 0
	v_mov_b32_e32 v67, 0
	v_mov_b32_e32 v68, 0
	v_mov_b32_e32 v69, 0
	v_mov_b32_e32 v70, 0
	v_mov_b32_e32 v71, 0
	v_mov_b32_e32 v72, 0
	v_mov_b32_e32 v73, 0
	v_mov_b32_e32 v74, 0
	v_mov_b32_e32 v75, 0
	v_mov_b32_e32 v76, 0
	v_mov_b32_e32 v77, 0
	v_cmp_lt_i32_e64 s[10:11], v50, v97
	v_mov_b32_e32 v91, v97
	v_and_b32_e32 v92, 3, v50
	s_waitcnt lgkmcnt(0)
	v_cndmask_b32_e64 v10, v11, v10, s[10:11]
	v_add_u32_e32 v92, 8, v92
	v_add_u32_e32 v93, -1, v97
	v_cndmask_b32_e64 v81, 0, v10, s[0:1]
	v_cndmask_b32_e64 v93, 0, v93, s[0:1]
	v_cndmask_b32_e64 v94, 0, v78, s[0:1]
	v_lshlrev_b32_e32 v81, 7, v81
	v_min_i32_e32 v116, v92, v93
	v_add_u32_e32 v117, 4, v92
	v_min_i32_e32 v117, v117, v93
	v_add_lshl_u32 v116, v116, v94, 2
	v_add_lshl_u32 v117, v117, v94, 2
	global_load_dword v87, v116, s[20:21]
	global_load_dword v88, v117, s[20:21]
	v_add_u32_e32 v92, 8, v92
	v_mov_b32_e32 v89, v81
	v_mov_b32_e32 v90, v81
	s_nop 1
	v_mov_b32_dpp v89, v81 row_shr:4 row_mask:0xf bank_mask:0xa
	v_mov_b32_dpp v90, v81 row_shl:4 row_mask:0xf bank_mask:0x5
	s_mov_b64 s[78:79], 0xff
	v_cmp_gt_i32_e64 s[44:45], v91, 0
	v_cmp_gt_i32_e64 s[46:47], v91, 1
	v_cmp_gt_i32_e64 s[48:49], v91, 2
	v_cmp_gt_i32_e64 s[50:51], v91, 3
	v_cmp_gt_i32_e64 s[52:53], v91, 4
	v_cmp_gt_i32_e64 s[54:55], v91, 5
	v_cmp_gt_i32_e64 s[56:57], v91, 6
	v_cmp_gt_i32_e64 s[58:59], v91, 7
	s_nop 0
	v_or_b32_dpp v79, v89, v56 quad_perm:[0,0,0,0] row_mask:0xf bank_mask:0xf
	v_or_b32_dpp v80, v89, v56 quad_perm:[1,1,1,1] row_mask:0xf bank_mask:0xf
	s_or_b64 exec, s[44:45], s[78:79]
	global_load_dwordx4 v[10:13], v79, s[24:25]
	global_load_dwordx4 v[14:17], v80, s[24:25]
	s_mov_b64 exec, -1
	s_nop 0
	v_or_b32_dpp v79, v89, v56 quad_perm:[2,2,2,2] row_mask:0xf bank_mask:0xf
	v_or_b32_dpp v80, v89, v56 quad_perm:[3,3,3,3] row_mask:0xf bank_mask:0xf
	s_or_b64 exec, s[48:49], s[78:79]
	global_load_dwordx4 v[18:21], v79, s[24:25]
	global_load_dwordx4 v[22:25], v80, s[24:25]
	s_mov_b64 exec, -1
	s_nop 0
	v_or_b32_dpp v79, v90, v56 quad_perm:[0,0,0,0] row_mask:0xf bank_mask:0xf
	v_or_b32_dpp v80, v90, v56 quad_perm:[1,1,1,1] row_mask:0xf bank_mask:0xf
	s_or_b64 exec, s[52:53], s[78:79]
	global_load_dwordx4 v[26:29], v79, s[24:25]
	global_load_dwordx4 v[30:33], v80, s[24:25]
	s_mov_b64 exec, -1
	s_nop 0
	v_or_b32_dpp v79, v90, v56 quad_perm:[2,2,2,2] row_mask:0xf bank_mask:0xf
	v_or_b32_dpp v80, v90, v56 quad_perm:[3,3,3,3] row_mask:0xf bank_mask:0xf
	s_or_b64 exec, s[56:57], s[78:79]
	global_load_dwordx4 v[34:37], v79, s[24:25]
	global_load_dwordx4 v[38:41], v80, s[24:25]
	s_mov_b64 exec, -1
	v_cmp_gt_i32_e64 s[60:61], v91, 8
	s_cmp_lg_u64 s[60:61], 0
	s_cbranch_scc0 .Lpl_last_a1
.Lpl_steady_a1:
	s_waitcnt vmcnt(6)
	v_lshlrev_b32_e32 v89, 7, v87
	v_lshlrev_b32_e32 v90, 7, v88
	v_min_i32_e32 v116, v92, v93
	v_add_u32_e32 v117, 4, v92
	v_min_i32_e32 v117, v117, v93
	v_add_lshl_u32 v116, v116, v94, 2
	v_add_lshl_u32 v117, v117, v94, 2
	global_load_dword v87, v116, s[20:21]
	global_load_dword v88, v117, s[20:21]
	v_add_u32_e32 v92, 8, v92
	v_cmp_gt_i32_e64 s[62:63], v91, 8
	v_cmp_gt_i32_e64 s[64:65], v91, 9
	v_cmp_gt_i32_e64 s[66:67], v91, 10
	v_cmp_gt_i32_e64 s[68:69], v91, 11
	v_cmp_gt_i32_e64 s[70:71], v91, 12
	v_cmp_gt_i32_e64 s[72:73], v91, 13
	v_cmp_gt_i32_e64 s[74:75], v91, 14
	v_cmp_gt_i32_e64 s[76:77], v91, 15
	s_mov_b64 exec, s[44:45]
	v_pk_minimum3_f16 v52, v52, v10, v14
	v_pk_maximum3_f16 v100, v100, v10, v14
	v_pk_minimum3_f16 v99, v99, v11, v15
	v_pk_maximum3_f16 v101, v101, v11, v15
	v_pk_minimum3_f16 v98, v98, v12, v16
	v_pk_maximum3_f16 v105, v105, v12, v16
	v_pk_minimum3_f16 v103, v103, v13, v17
	v_pk_maximum3_f16 v104, v104, v13, v17
	v_pk_mul_f16 v110, v10, v10
	v_mov_b32_e32 v106, v10
	v_pk_mul_f16 v111, v11, v11
	v_mov_b32_e32 v107, v11
	v_pk_mul_f16 v112, v12, v12
	v_mov_b32_e32 v108, v12
	v_pk_mul_f16 v113, v13, v13
	v_mov_b32_e32 v109, v13
	s_mov_b64 exec, s[46:47]
	v_pk_add_f16 v106, v106, v14
	v_pk_fma_f16 v110, v14, v14, v110
	v_pk_add_f16 v107, v107, v15
	v_pk_fma_f16 v111, v15, v15, v111
	v_pk_add_f16 v108, v108, v16
	v_pk_fma_f16 v112, v16, v16, v112
	v_pk_add_f16 v109, v109, v17
	v_pk_fma_f16 v113, v17, v17, v113
	s_mov_b64 exec, -1
	s_nop 0
	v_or_b32_dpp v79, v89, v56 quad_perm:[0,0,0,0] row_mask:0xf bank_mask:0xf
	v_or_b32_dpp v80, v89, v56 quad_perm:[1,1,1,1] row_mask:0xf bank_mask:0xf
	s_or_b64 exec, s[62:63], s[78:79]
	global_load_dwordx4 v[10:13], v79, s[24:25]
	global_load_dwordx4 v[14:17], v80, s[24:25]
	s_mov_b64 exec, -1
	s_waitcnt vmcnt(8)
	s_mov_b64 exec, s[48:49]
	v_pk_minimum3_f16 v52, v52, v18, v22
	v_pk_maximum3_f16 v100, v100, v18, v22
	v_pk_minimum3_f16 v99, v99, v19, v23
	v_pk_maximum3_f16 v101, v101, v19, v23
	v_pk_minimum3_f16 v98, v98, v20, v24
	v_pk_maximum3_f16 v105, v105, v20, v24
	v_pk_minimum3_f16 v103, v103, v21, v25
	v_pk_maximum3_f16 v104, v104, v21, v25
	v_pk_add_f16 v106, v106, v18
	v_pk_fma_f16 v110, v18, v18, v110
	v_pk_add_f16 v107, v107, v19
	v_pk_fma_f16 v111, v19, v19, v111
	v_pk_add_f16 v108, v108, v20
	v_pk_fma_f16 v112, v20, v20, v112
	v_pk_add_f16 v109, v109, v21
	v_pk_fma_f16 v113, v21, v21, v113
	s_mov_b64 exec, s[50:51]
	v_pk_add_f16 v106, v106, v22
	v_pk_fma_f16 v110, v22, v22, v110
	v_pk_add_f16 v107, v107, v23
	v_pk_fma_f16 v111, v23, v23, v111
	v_pk_add_f16 v108, v108, v24
	v_pk_fma_f16 v112, v24, v24, v112
	v_pk_add_f16 v109, v109, v25
	v_pk_fma_f16 v113, v25, v25, v113
	s_mov_b64 exec, -1
	s_nop 0
	v_or_b32_dpp v79, v89, v56 quad_perm:[2,2,2,2] row_mask:0xf bank_mask:0xf
	v_or_b32_dpp v80, v89, v56 quad_perm:[3,3,3,3] row_mask:0xf bank_mask:0xf
	s_or_b64 exec, s[66:67], s[78:79]
	global_load_dwordx4 v[18:21], v79, s[24:25]
	global_load_dwordx4 v[22:25], v80, s[24:25]
	s_mov_b64 exec, -1
	s_waitcnt vmcnt(8)
	s_mov_b64 exec, s[52:53]
	v_pk_minimum3_f16 v52, v52, v26, v30
	v_pk_maximum3_f16 v100, v100, v26, v30
	v_pk_minimum3_f16 v99, v99, v27, v31
	v_pk_maximum3_f16 v101, v101, v27, v31
	v_pk_minimum3_f16 v98, v98, v28, v32
	v_pk_maximum3_f16 v105, v105, v28, v32
	v_pk_minimum3_f16 v103, v103, v29, v33
	v_pk_maximum3_f16 v104, v104, v29, v33
	v_pk_add_f16 v106, v106, v26
	v_pk_fma_f16 v110, v26, v26, v110
	v_pk_add_f16 v107, v107, v27
	v_pk_fma_f16 v111, v27, v27, v111
	v_pk_add_f16 v108, v108, v28
	v_pk_fma_f16 v112, v28, v28, v112
	v_pk_add_f16 v109, v109, v29
	v_pk_fma_f16 v113, v29, v29, v113
	s_mov_b64 exec, s[54:55]
	v_pk_add_f16 v106, v106, v30
	v_pk_fma_f16 v110, v30, v30, v110
	v_pk_add_f16 v107, v107, v31
	v_pk_fma_f16 v111, v31, v31, v111
	v_pk_add_f16 v108, v108, v32
	v_pk_fma_f16 v112, v32, v32, v112
	v_pk_add_f16 v109, v109, v33
	v_pk_fma_f16 v113, v33, v33, v113
	s_mov_b64 exec, -1
	s_nop 0
	v_or_b32_dpp v79, v90, v56 quad_perm:[0,0,0,0] row_mask:0xf bank_mask:0xf
	v_or_b32_dpp v80, v90, v56 quad_perm:[1,1,1,1] row_mask:0xf bank_mask:0xf
	s_or_b64 exec, s[70:71], s[78:79]
	global_load_dwordx4 v[26:29], v79, s[24:25]
	global_load_dwordx4 v[30:33], v80, s[24:25]
	s_mov_b64 exec, -1
	s_waitcnt vmcnt(8)
	s_mov_b64 exec, s[56:57]
	v_pk_minimum3_f16 v52, v52, v34, v38
	v_pk_maximum3_f16 v100, v100, v34, v38
	v_pk_minimum3_f16 v99, v99, v35, v39
	v_pk_maximum3_f16 v101, v101, v35, v39
	v_pk_minimum3_f16 v98, v98, v36, v40
	v_pk_maximum3_f16 v105, v105, v36, v40
	v_pk_minimum3_f16 v103, v103, v37, v41
	v_pk_maximum3_f16 v104, v104, v37, v41
	v_pk_add_f16 v106, v106, v34
	v_pk_fma_f16 v110, v34, v34, v110
	v_pk_add_f16 v107, v107, v35
	v_pk_fma_f16 v111, v35, v35, v111
	v_pk_add_f16 v108, v108, v36
	v_pk_fma_f16 v112, v36, v36, v112
	v_pk_add_f16 v109, v109, v37
	v_pk_fma_f16 v113, v37, v37, v113
	s_mov_b64 exec, s[58:59]
	v_pk_add_f16 v106, v106, v38
	v_pk_fma_f16 v110, v38, v38, v110
	v_pk_add_f16 v107, v107, v39
	v_pk_fma_f16 v111, v39, v39, v111
	v_pk_add_f16 v108, v108, v40
	v_pk_fma_f16 v112, v40, v40, v112
	v_pk_add_f16 v109, v109, v41
	v_pk_fma_f16 v113, v41, v41, v113
	s_mov_b64 exec, -1
	s_nop 0
	v_or_b32_dpp v79, v90, v56 quad_perm:[2,2,2,2] row_mask:0xf bank_mask:0xf
	v_or_b32_dpp v80, v90, v56 quad_perm:[3,3,3,3] row_mask:0xf bank_mask:0xf
	s_or_b64 exec, s[74:75], s[78:79]
	global_load_dwordx4 v[34:37], v79, s[24:25]
	global_load_dwordx4 v[38:41], v80, s[24:25]
	s_mov_b64 exec, -1
	s_mov_b64 exec, s[44:45]
	v_cvt_f32_f16_e32 v114, v106
	v_cvt_f32_f16_sdwa v115, v106 dst_sel:DWORD dst_unused:UNUSED_PAD src0_sel:WORD_1
	v_cvt_f32_f16_e32 v118, v110
	v_cvt_f32_f16_sdwa v119, v110 dst_sel:DWORD dst_unused:UNUSED_PAD src0_sel:WORD_1
	v_pk_add_f32 v[72:73], v[72:73], v[114:115]
	v_cvt_f32_f16_e32 v114, v107
	v_cvt_f32_f16_sdwa v115, v107 dst_sel:DWORD dst_unused:UNUSED_PAD src0_sel:WORD_1
	v_pk_add_f32 v[76:77], v[76:77], v[118:119]
	v_cvt_f32_f16_e32 v118, v111
	v_cvt_f32_f16_sdwa v119, v111 dst_sel:DWORD dst_unused:UNUSED_PAD src0_sel:WORD_1
	v_pk_add_f32 v[70:71], v[70:71], v[114:115]
	v_cvt_f32_f16_e32 v114, v108
	v_cvt_f32_f16_sdwa v115, v108 dst_sel:DWORD dst_unused:UNUSED_PAD src0_sel:WORD_1
	v_pk_add_f32 v[74:75], v[74:75], v[118:119]
	v_cvt_f32_f16_e32 v118, v112
	v_cvt_f32_f16_sdwa v119, v112 dst_sel:DWORD dst_unused:UNUSED_PAD src0_sel:WORD_1
	v_pk_add_f32 v[64:65], v[64:65], v[114:115]
	v_cvt_f32_f16_e32 v114, v109
	v_cvt_f32_f16_sdwa v115, v109 dst_sel:DWORD dst_unused:UNUSED_PAD src0_sel:WORD_1
	v_pk_add_f32 v[68:69], v[68:69], v[118:119]
	v_cvt_f32_f16_e32 v118, v113
	v_cvt_f32_f16_sdwa v119, v113 dst_sel:DWORD dst_unused:UNUSED_PAD src0_sel:WORD_1
	v_pk_add_f32 v[62:63], v[62:63], v[114:115]
	s_nop 0
	v_pk_add_f32 v[66:67], v[66:67], v[118:119]
	s_mov_b64 exec, -1
	s_mov_b64 s[44:45], s[62:63]
	s_mov_b64 s[46:47], s[64:65]
	s_mov_b64 s[48:49], s[66:67]
	s_mov_b64 s[50:51], s[68:69]
	s_mov_b64 s[52:53], s[70:71]
	s_mov_b64 s[54:55], s[72:73]
	s_mov_b64 s[56:57], s[74:75]
	s_mov_b64 s[58:59], s[76:77]
	v_add_u32_e32 v91, -8, v91
	v_cmp_gt_i32_e64 s[60:61], v91, 8
	s_cmp_lg_u64 s[60:61], 0
	s_cbranch_scc1 .Lpl_steady_a1
